# gemm prologue reorder + barrier leader reorder + 20-byte body shift
# speedup vs baseline: 1.0018x; 1.0018x over previous
_Z10fwd_kernel6Params:
	s_mov_b64 s[88:89], s[0:1]
	s_nop 0
	s_nop 0
	s_nop 0
	s_nop 0
	s_nop 0
	s_load_dword s74, s[0:1], 0x98
	s_add_u32 s0, s88, 0x98
	s_addc_u32 s1, s89, 0
	v_lshl_add_u32 v1, v0, 2, 0
	v_writelane_b32 v253, s0, 0
	v_add_u32_e32 v1, 0x24000, v1
	v_mov_b32_e32 v2, 0
	s_mov_b32 s87, s2
	v_writelane_b32 v253, s1, 1
	ds_write2st64_b32 v1, v2, v2 offset1:8
	ds_write2st64_b32 v1, v2, v2 offset0:16 offset1:24
	v_or_b32_e32 v1, 0x800, v0
	s_mov_b64 s[0:1], -1
	s_and_saveexec_b64 s[2:3], s[0:1]
	v_lshl_add_u32 v3, v1, 2, 0
	v_add_u32_e32 v3, 0x24000, v3
	ds_write_b32 v3, v2
	s_or_b64 exec, exec, s[2:3]
	s_and_saveexec_b64 s[2:3], s[0:1]
	s_add_i32 s0, 0, 0x24000
	v_lshl_add_u32 v1, v1, 2, s0
	v_mov_b32_e32 v2, 0
	ds_write_b32 v1, v2 offset:2048
	s_or_b64 exec, exec, s[2:3]
	s_load_dwordx2 s[0:1], s[88:89], 0x88
	v_or_b32_e32 v1, 0xc00, v0
	v_cmp_gt_u32_e64 s[2:3], 7, 6
	v_cmp_gt_u32_e64 s[6:7], 7, 5
	s_and_saveexec_b64 s[4:5], s[6:7]
	v_lshl_add_u32 v2, v1, 2, 0
	v_add_u32_e32 v2, 0x24000, v2
	v_mov_b32_e32 v3, 0
	ds_write_b32 v2, v3
	s_or_b64 exec, exec, s[4:5]
	s_load_dwordx2 s[50:51], s[88:89], 0x90
	s_and_saveexec_b64 s[4:5], s[2:3]
	s_add_i32 s2, 0, 0x24000
	v_lshl_add_u32 v1, v1, 2, s2
	v_mov_b32_e32 v2, 0
	ds_write_b32 v1, v2 offset:2048
	s_or_b64 exec, exec, s[4:5]
	s_waitcnt lgkmcnt(0)
	s_barrier
	s_add_u32 s26, s0, 0x4000
	s_getreg_b32 s2, hwreg(HW_REG_XCC_ID, 0, 4)
	s_addc_u32 s27, s1, 0
	s_and_b32 s33, s2, 15
	v_cmp_eq_u32_e64 s[4:5], 0, v0
	s_mov_b64 s[2:3], exec
	s_nop 0
	v_writelane_b32 v253, s4, 2
	s_nop 1
	v_writelane_b32 v253, s5, 3
	s_and_b64 s[4:5], s[2:3], s[4:5]
	s_mov_b64 exec, s[4:5]
	s_cbranch_execz .LBB0_11
	s_mov_b64 s[4:5], exec
	v_mbcnt_lo_u32_b32 v1, s4, 0
	v_mbcnt_hi_u32_b32 v1, s5, v1
	v_cmp_eq_u32_e32 vcc, 0, v1
	s_and_b64 s[6:7], exec, vcc
	s_mov_b64 exec, s[6:7]
	s_cbranch_execz .LBB0_11
	s_lshl_b32 s6, s33, 8
	s_bcnt1_i32_b64 s4, s[4:5]
	v_mov_b32_e32 v1, s6
	v_mov_b32_e32 v2, s4
	global_atomic_add v1, v2, s[26:27] offset:1024
